# wide8 QK^T: all eight K-fragment LDS reads issued before the first MFMA (second d-chunk staged in the p1 accumulator registers), on top of v11
# baseline (speedup 1.0000x reference)
; #define SBAR() __builtin_amdgcn_sched_barrier(0)
; __device__ __forceinline__ void mask_tile_perm(f32x16& p0, f32x16& p1, int dq) {
;     const float NEG = -__builtin_inff();
; #pragma unroll
;     for (int r = 0; r < 16; ++r) { const int c = 16 * (r & 3) + (r >> 2);
;         if (dq - c < 0) p0[r] = NEG;
;         if (dq - c - 4 < 0) p1[r] = NEG; }
; }
; template <int KB, bool LOWREG = false>
; __device__ __forceinline__ void qkt_f8(f32x16& p0, f32x16& p1, const char* K_lds, int r32, int hi, const i32x8 (&q8)[2]) {
;     asm volatile("" : "+v"(r32), "+v"(hi));
;     typedef const __attribute__((address_space(3))) bf16x8* lds_f;
;     const unsigned sw = (unsigned)((r32 >> 1) & 7), base = (unsigned)(__UINTPTR_TYPE__)K_lds + (unsigned)(r32 * 128) + (unsigned)(KB * SHM_K);
;     if constexpr (LOWREG) {
;     ...
;         i32x8 f0 = KF8(0, 0), f1 = KF8(0, 1);
;         SBAR();
;         asm volatile("v_mfma_f32_32x32x64_f8f6f4 %0, %1, %2, 0" : "=&v"(p0) : "v"(f0), "v"(q8[0]));
;         asm volatile("v_mfma_f32_32x32x64_f8f6f4 %0, %1, %2, 0" : "=&v"(p1) : "v"(f1), "v"(q8[0]));
;         SBAR();
;         f0 = KF8(1, 0); f1 = KF8(1, 1);
;         SBAR();
;         asm volatile("v_mfma_f32_32x32x64_f8f6f4 %0, %1, %2, %0" : "+v"(p0) : "v"(f0), "v"(q8[1]));
;         asm volatile("v_mfma_f32_32x32x64_f8f6f4 %0, %1, %2, %0" : "+v"(p1) : "v"(f1), "v"(q8[1]));
;         asm volatile("s_nop 15\n\ts_nop 15" ::: "memory");
;         SBAR();
;     ...
;         return;
.LBB0_1213:
	s_setprio 1
	v_mov_b32_e32 v2, v213
	v_mov_b32_e32 v4, v202
	s_add_i32 s76, 0, 0x10000
	s_cmp_lg_u32 s76, -1
	v_lshrrev_b32_e32 v12, 1, v4
	s_cselect_b32 s6, s76, 0
	v_lshlrev_b32_e32 v2, 1, v2
	v_bfe_u32 v5, v4, 1, 3
	v_lshl_add_u32 v13, v4, 7, s6
	v_bitop3_b32 v4, v12, v2, 7 bitop3:0x6c
	v_lshl_add_u32 v8, v4, 4, v13
	v_bitop3_b32 v4, v2, v5, 1 bitop3:0x36
	v_lshl_add_u32 v14, v4, 4, v13
	v_add_u32_e32 v4, 4, v2
	v_bitop3_b32 v4, v4, v12, 7 bitop3:0x78
	v_add_u32_e32 v2, 5, v2
	v_lshl_add_u32 v162, v4, 4, v13
	v_bitop3_b32 v2, v2, v12, 7 bitop3:0x78
	v_lshl_add_u32 v163, v2, 4, v13
	ds_read_b128 v[4:7], v8
	ds_read_b128 v[242:245], v8 offset:4096
	ds_read_b128 v[8:11], v14
	ds_read_b128 v[246:249], v14 offset:4096
	ds_read_b128 v[146:149], v162
	ds_read_b128 v[154:157], v162 offset:4096
	ds_read_b128 v[150:153], v163
	ds_read_b128 v[158:161], v163 offset:4096
	s_waitcnt lgkmcnt(4)
	v_mfma_f32_32x32x64_f8f6f4 v[162:177], v[4:11], v[178:185], 0
	s_waitcnt lgkmcnt(0)
	v_mfma_f32_32x32x64_f8f6f4 v[162:177], v[146:153], v[186:193], v[162:177]
	v_mov_b32_e32 v4, v154
	v_mov_b32_e32 v5, v155
	v_mov_b32_e32 v6, v156
	v_mov_b32_e32 v7, v157
	v_mov_b32_e32 v8, v158
	v_mov_b32_e32 v9, v159
	v_mov_b32_e32 v10, v160
	v_mov_b32_e32 v11, v161
	s_nop 0
	v_mfma_f32_32x32x64_f8f6f4 v[146:161], v[242:249], v[178:185], 0
	v_mfma_f32_32x32x64_f8f6f4 v[146:161], v[4:11], v[186:193], v[146:161]
	s_nop 15
	s_nop 5
	s_cmp_le_i32 s78, s80
	s_cbranch_scc1 .LBB0_1215
	v_cmp_gt_i32_e64 s[58:59], 50, v240
	v_cmp_gt_i32_e64 s[66:67], 51, v240
	v_cmp_gt_i32_e64 s[50:51], 49, v240
	s_and_b64 s[58:59], s[66:67], s[58:59]
	v_cmp_gt_i32_e64 s[42:43], 48, v240
	s_and_b64 s[50:51], s[58:59], s[50:51]
	v_cmp_gt_i32_e64 s[40:41], 32, v240
	s_and_b64 s[42:43], s[50:51], s[42:43]
	v_cmp_gt_i32_e64 s[38:39], 16, v240
	s_and_b64 s[40:41], s[42:43], s[40:41]
	v_cmp_gt_i32_e64 s[36:37], 0, v240
	s_and_b64 s[38:39], s[40:41], s[38:39]
	s_and_b64 s[36:37], s[38:39], s[36:37]
	v_cmp_gt_i32_e64 s[28:29], 54, v240
	v_cndmask_b32_e64 v162, v162, v210, s[36:37]
	v_cmp_gt_i32_e64 s[36:37], 55, v240
	v_cmp_gt_i32_e64 s[20:21], 53, v240
	s_and_b64 s[28:29], s[36:37], s[28:29]
	v_cmp_gt_i32_e64 s[12:13], 52, v240
	s_and_b64 s[20:21], s[28:29], s[20:21]
	v_cmp_gt_i32_e64 s[8:9], 36, v240
	v_cmp_gt_i32_e64 s[48:49], 33, v240
	v_cmp_gt_i32_e64 s[16:17], 37, v240
	v_cmp_gt_i32_e64 s[56:57], 34, v240
	v_cmp_gt_i32_e64 s[24:25], 38, v240
	v_cmp_gt_i32_e64 s[64:65], 35, v240
	v_cmp_gt_i32_e64 s[34:35], 39, v240
	s_and_b64 s[12:13], s[20:21], s[12:13]
	v_cmp_gt_i32_e64 s[6:7], 20, v240
	v_cmp_gt_i32_e64 s[46:47], 17, v240
	v_cmp_gt_i32_e64 s[14:15], 21, v240
	v_cmp_gt_i32_e64 s[54:55], 18, v240
	v_cmp_gt_i32_e64 s[22:23], 22, v240
	v_cmp_gt_i32_e64 s[62:63], 19, v240
	v_cmp_gt_i32_e64 s[30:31], 23, v240
	s_and_b64 s[64:65], s[66:67], s[64:65]
	s_and_b64 s[56:57], s[58:59], s[56:57]
	s_and_b64 s[48:49], s[50:51], s[48:49]
	s_and_b64 s[34:35], s[36:37], s[34:35]
	s_and_b64 s[24:25], s[28:29], s[24:25]
	s_and_b64 s[16:17], s[20:21], s[16:17]
	s_and_b64 s[8:9], s[12:13], s[8:9]
	v_cmp_gt_i32_e32 vcc, 4, v240
	v_cmp_gt_i32_e64 s[44:45], 1, v240
	v_cmp_gt_i32_e64 s[10:11], 5, v240
	v_cmp_gt_i32_e64 s[52:53], 2, v240
	v_cmp_gt_i32_e64 s[18:19], 6, v240
	v_cmp_gt_i32_e64 s[60:61], 3, v240
	v_cmp_gt_i32_e64 s[26:27], 7, v240
	s_and_b64 s[62:63], s[64:65], s[62:63]
	s_and_b64 s[54:55], s[56:57], s[54:55]
	s_and_b64 s[46:47], s[48:49], s[46:47]
	s_and_b64 s[30:31], s[34:35], s[30:31]
	s_and_b64 s[22:23], s[24:25], s[22:23]
	s_and_b64 s[14:15], s[16:17], s[14:15]
	s_and_b64 s[6:7], s[8:9], s[6:7]
	v_cndmask_b32_e64 v173, v173, v210, s[58:59]
	v_cndmask_b32_e64 v169, v169, v210, s[50:51]
	s_and_b64 s[58:59], s[62:63], s[60:61]
	v_cndmask_b32_e64 v165, v165, v210, s[42:43]
	s_and_b64 s[50:51], s[54:55], s[52:53]
	s_and_b64 s[42:43], s[46:47], s[44:45]
	s_and_b64 s[26:27], s[30:31], s[26:27]
	s_and_b64 s[18:19], s[22:23], s[18:19]
	s_and_b64 s[10:11], s[14:15], s[10:11]
	s_and_b64 vcc, s[6:7], vcc
	v_cndmask_b32_e64 v177, v177, v210, s[66:67]
	v_cndmask_b32_e64 v176, v176, v210, s[64:65]
	v_cndmask_b32_e64 v175, v175, v210, s[62:63]
	v_cndmask_b32_e64 v172, v172, v210, s[56:57]
	v_cndmask_b32_e64 v174, v174, v210, s[58:59]
	v_cndmask_b32_e64 v171, v171, v210, s[54:55]
	v_cndmask_b32_e64 v168, v168, v210, s[48:49]
	v_cndmask_b32_e64 v170, v170, v210, s[50:51]
	v_cndmask_b32_e64 v167, v167, v210, s[46:47]
	v_cndmask_b32_e64 v164, v164, v210, s[40:41]
	v_cndmask_b32_e64 v166, v166, v210, s[42:43]
	v_cndmask_b32_e64 v163, v163, v210, s[38:39]
	v_cndmask_b32_e64 v161, v161, v210, s[36:37]
	v_cndmask_b32_e64 v160, v160, v210, s[34:35]
	v_cndmask_b32_e64 v157, v157, v210, s[28:29]
	v_cndmask_b32_e64 v159, v159, v210, s[30:31]
	v_cndmask_b32_e64 v156, v156, v210, s[24:25]
	v_cndmask_b32_e64 v153, v153, v210, s[20:21]
	v_cndmask_b32_e64 v158, v158, v210, s[26:27]
	v_cndmask_b32_e64 v155, v155, v210, s[22:23]
	v_cndmask_b32_e64 v152, v152, v210, s[16:17]
	v_cndmask_b32_e64 v149, v149, v210, s[12:13]
	v_cndmask_b32_e64 v154, v154, v210, s[18:19]
	v_cndmask_b32_e64 v151, v151, v210, s[14:15]
	v_cndmask_b32_e64 v148, v148, v210, s[8:9]
	v_cndmask_b32_e64 v150, v150, v210, s[10:11]
	v_cndmask_b32_e64 v147, v147, v210, s[6:7]
	v_cndmask_b32_e32 v146, v146, v210, vcc

; #define SBAR() __builtin_amdgcn_sched_barrier(0)
; __device__ __forceinline__ void mask_tile_perm(f32x16& p0, f32x16& p1, int dq) {
;     const float NEG = -__builtin_inff();
; #pragma unroll
;     for (int r = 0; r < 16; ++r) { const int c = 16 * (r & 3) + (r >> 2);
;         if (dq - c < 0) p0[r] = NEG;
;         if (dq - c - 4 < 0) p1[r] = NEG; }
; }
; template <int KB, bool LOWREG = false>
; __device__ __forceinline__ void qkt_f8(f32x16& p0, f32x16& p1, const char* K_lds, int r32, int hi, const i32x8 (&q8)[2]) {
;     asm volatile("" : "+v"(r32), "+v"(hi));
;     typedef const __attribute__((address_space(3))) bf16x8* lds_f;
;     const unsigned sw = (unsigned)((r32 >> 1) & 7), base = (unsigned)(__UINTPTR_TYPE__)K_lds + (unsigned)(r32 * 128) + (unsigned)(KB * SHM_K);
;     if constexpr (LOWREG) {
;     ...
;         i32x8 f0 = KF8(0, 0), f1 = KF8(0, 1);
;         SBAR();
;         asm volatile("v_mfma_f32_32x32x64_f8f6f4 %0, %1, %2, 0" : "=&v"(p0) : "v"(f0), "v"(q8[0]));
;         asm volatile("v_mfma_f32_32x32x64_f8f6f4 %0, %1, %2, 0" : "=&v"(p1) : "v"(f1), "v"(q8[0]));
;         SBAR();
;         f0 = KF8(1, 0); f1 = KF8(1, 1);
;         SBAR();
;         asm volatile("v_mfma_f32_32x32x64_f8f6f4 %0, %1, %2, %0" : "+v"(p0) : "v"(f0), "v"(q8[1]));
;         asm volatile("v_mfma_f32_32x32x64_f8f6f4 %0, %1, %2, %0" : "+v"(p1) : "v"(f1), "v"(q8[1]));
;         asm volatile("s_nop 15\n\ts_nop 15" ::: "memory");
;         SBAR();
;     ...
;         return;
.LBB0_1231:
	s_setprio 1
	s_cmp_lg_u32 s76, -1
	v_mov_b32_e32 v4, v213
	v_mov_b32_e32 v5, v202
	s_cselect_b32 s6, s76, 0
	s_addk_i32 s6, 0x4000
	v_lshrrev_b32_e32 v12, 1, v5
	v_lshlrev_b32_e32 v14, 1, v4
	v_bfe_u32 v6, v5, 1, 3
	v_lshl_add_u32 v13, v5, 7, s6
	v_bitop3_b32 v4, v12, v14, 7 bitop3:0x6c
	v_lshl_add_u32 v8, v4, 4, v13
	v_bitop3_b32 v4, v14, v6, 1 bitop3:0x36
	v_lshl_add_u32 v15, v4, 4, v13
	v_add_u32_e32 v4, 4, v14
	v_bitop3_b32 v4, v4, v12, 7 bitop3:0x78
	v_lshl_add_u32 v162, v4, 4, v13
	v_add_u32_e32 v4, 5, v14
	v_bitop3_b32 v4, v4, v12, 7 bitop3:0x78
	v_lshl_add_u32 v163, v4, 4, v13
	ds_read_b128 v[4:7], v8
	ds_read_b128 v[244:247], v8 offset:4096
	ds_read_b128 v[8:11], v15
	ds_read_b128 v[248:251], v15 offset:4096
	ds_read_b128 v[146:149], v162
	ds_read_b128 v[154:157], v162 offset:4096
	ds_read_b128 v[150:153], v163
	ds_read_b128 v[158:161], v163 offset:4096
	s_waitcnt lgkmcnt(4)
	v_mfma_f32_32x32x64_f8f6f4 v[162:177], v[4:11], v[178:185], 0
	s_waitcnt lgkmcnt(0)
	v_mfma_f32_32x32x64_f8f6f4 v[162:177], v[146:153], v[186:193], v[162:177]
	v_mov_b32_e32 v4, v154
	v_mov_b32_e32 v5, v155
	v_mov_b32_e32 v6, v156
	v_mov_b32_e32 v7, v157
	v_mov_b32_e32 v8, v158
	v_mov_b32_e32 v9, v159
	v_mov_b32_e32 v10, v160
	v_mov_b32_e32 v11, v161
	s_nop 0
	v_mfma_f32_32x32x64_f8f6f4 v[146:161], v[244:251], v[178:185], 0
	v_mfma_f32_32x32x64_f8f6f4 v[146:161], v[4:11], v[186:193], v[146:161]
	s_nop 15
	s_nop 5
	s_add_i32 s6, s78, 64
	s_cmp_le_i32 s6, s80
	s_cbranch_scc1 .LBB0_1233
	v_subrev_u32_e32 v4, 64, v240
	v_cmp_gt_i32_e64 s[58:59], 50, v4
	v_cmp_gt_i32_e64 s[66:67], 51, v4
	v_cmp_gt_i32_e64 s[50:51], 49, v4
	s_and_b64 s[58:59], s[66:67], s[58:59]
	v_cmp_gt_i32_e64 s[42:43], 48, v4
	s_and_b64 s[50:51], s[58:59], s[50:51]
	v_cmp_gt_i32_e64 s[40:41], 32, v4
	s_and_b64 s[42:43], s[50:51], s[42:43]
	v_cmp_gt_i32_e64 s[38:39], 16, v4
	s_and_b64 s[40:41], s[42:43], s[40:41]
	v_cmp_gt_i32_e64 s[36:37], 0, v4
	s_and_b64 s[38:39], s[40:41], s[38:39]
	s_and_b64 s[36:37], s[38:39], s[36:37]
	v_cmp_gt_i32_e64 s[28:29], 54, v4
	v_cndmask_b32_e64 v162, v162, v210, s[36:37]
	v_cmp_gt_i32_e64 s[36:37], 55, v4
	v_cmp_gt_i32_e64 s[20:21], 53, v4
	s_and_b64 s[28:29], s[36:37], s[28:29]
	v_cmp_gt_i32_e64 s[12:13], 52, v4
	s_and_b64 s[20:21], s[28:29], s[20:21]
	v_cmp_gt_i32_e64 s[8:9], 36, v4
	v_cmp_gt_i32_e64 s[48:49], 33, v4
	v_cmp_gt_i32_e64 s[16:17], 37, v4
	v_cmp_gt_i32_e64 s[56:57], 34, v4
	v_cmp_gt_i32_e64 s[24:25], 38, v4
	v_cmp_gt_i32_e64 s[64:65], 35, v4
	v_cmp_gt_i32_e64 s[34:35], 39, v4
	s_and_b64 s[12:13], s[20:21], s[12:13]
	v_cmp_gt_i32_e64 s[6:7], 20, v4
	v_cmp_gt_i32_e64 s[46:47], 17, v4
	v_cmp_gt_i32_e64 s[14:15], 21, v4
	v_cmp_gt_i32_e64 s[54:55], 18, v4
	v_cmp_gt_i32_e64 s[22:23], 22, v4
	v_cmp_gt_i32_e64 s[62:63], 19, v4
	v_cmp_gt_i32_e64 s[30:31], 23, v4
	s_and_b64 s[64:65], s[66:67], s[64:65]
	s_and_b64 s[56:57], s[58:59], s[56:57]
	s_and_b64 s[48:49], s[50:51], s[48:49]
	s_and_b64 s[34:35], s[36:37], s[34:35]
	s_and_b64 s[24:25], s[28:29], s[24:25]
	s_and_b64 s[16:17], s[20:21], s[16:17]
	s_and_b64 s[8:9], s[12:13], s[8:9]
	v_cmp_gt_i32_e32 vcc, 4, v4
	v_cmp_gt_i32_e64 s[44:45], 1, v4
	v_cmp_gt_i32_e64 s[10:11], 5, v4
	v_cmp_gt_i32_e64 s[52:53], 2, v4
	v_cmp_gt_i32_e64 s[18:19], 6, v4
	v_cmp_gt_i32_e64 s[60:61], 3, v4
	v_cmp_gt_i32_e64 s[26:27], 7, v4
	s_and_b64 s[62:63], s[64:65], s[62:63]
	s_and_b64 s[54:55], s[56:57], s[54:55]
	s_and_b64 s[46:47], s[48:49], s[46:47]
	s_and_b64 s[30:31], s[34:35], s[30:31]
	s_and_b64 s[22:23], s[24:25], s[22:23]
	s_and_b64 s[14:15], s[16:17], s[14:15]
	s_and_b64 s[6:7], s[8:9], s[6:7]
	v_cndmask_b32_e64 v173, v173, v210, s[58:59]
	v_cndmask_b32_e64 v169, v169, v210, s[50:51]
	s_and_b64 s[58:59], s[62:63], s[60:61]
	v_cndmask_b32_e64 v165, v165, v210, s[42:43]
	s_and_b64 s[50:51], s[54:55], s[52:53]
	s_and_b64 s[42:43], s[46:47], s[44:45]
	s_and_b64 s[26:27], s[30:31], s[26:27]
	s_and_b64 s[18:19], s[22:23], s[18:19]
	s_and_b64 s[10:11], s[14:15], s[10:11]
	s_and_b64 vcc, s[6:7], vcc
	v_cndmask_b32_e64 v177, v177, v210, s[66:67]
	v_cndmask_b32_e64 v176, v176, v210, s[64:65]
	v_cndmask_b32_e64 v175, v175, v210, s[62:63]
	v_cndmask_b32_e64 v172, v172, v210, s[56:57]
	v_cndmask_b32_e64 v174, v174, v210, s[58:59]
	v_cndmask_b32_e64 v171, v171, v210, s[54:55]
	v_cndmask_b32_e64 v168, v168, v210, s[48:49]
	v_cndmask_b32_e64 v170, v170, v210, s[50:51]
	v_cndmask_b32_e64 v167, v167, v210, s[46:47]
	v_cndmask_b32_e64 v164, v164, v210, s[40:41]
	v_cndmask_b32_e64 v166, v166, v210, s[42:43]
	v_cndmask_b32_e64 v163, v163, v210, s[38:39]
	v_cndmask_b32_e64 v161, v161, v210, s[36:37]
	v_cndmask_b32_e64 v160, v160, v210, s[34:35]
	v_cndmask_b32_e64 v157, v157, v210, s[28:29]
	v_cndmask_b32_e64 v159, v159, v210, s[30:31]
	v_cndmask_b32_e64 v156, v156, v210, s[24:25]
	v_cndmask_b32_e64 v153, v153, v210, s[20:21]
	v_cndmask_b32_e64 v158, v158, v210, s[26:27]
	v_cndmask_b32_e64 v155, v155, v210, s[22:23]
	v_cndmask_b32_e64 v152, v152, v210, s[16:17]
	v_cndmask_b32_e64 v149, v149, v210, s[12:13]
	v_cndmask_b32_e64 v154, v154, v210, s[18:19]
	v_cndmask_b32_e64 v151, v151, v210, s[14:15]
	v_cndmask_b32_e64 v148, v148, v210, s[8:9]
	v_cndmask_b32_e64 v150, v150, v210, s[10:11]
	v_cndmask_b32_e64 v147, v147, v210, s[6:7]
	v_cndmask_b32_e32 v146, v146, v210, vcc

; #define SBAR() __builtin_amdgcn_sched_barrier(0)
; __device__ __forceinline__ void mask_tile_perm(f32x16& p0, f32x16& p1, int dq) {
;     const float NEG = -__builtin_inff();
; #pragma unroll
;     for (int r = 0; r < 16; ++r) { const int c = 16 * (r & 3) + (r >> 2);
;         if (dq - c < 0) p0[r] = NEG;
;         if (dq - c - 4 < 0) p1[r] = NEG; }
; }
; template <int KB, bool LOWREG = false>
; __device__ __forceinline__ void qkt_f8(f32x16& p0, f32x16& p1, const char* K_lds, int r32, int hi, const i32x8 (&q8)[2]) {
;     asm volatile("" : "+v"(r32), "+v"(hi));
;     typedef const __attribute__((address_space(3))) bf16x8* lds_f;
;     const unsigned sw = (unsigned)((r32 >> 1) & 7), base = (unsigned)(__UINTPTR_TYPE__)K_lds + (unsigned)(r32 * 128) + (unsigned)(KB * SHM_K);
;     if constexpr (LOWREG) {
;     ...
;         i32x8 f0 = KF8(0, 0), f1 = KF8(0, 1);
;         SBAR();
;         asm volatile("v_mfma_f32_32x32x64_f8f6f4 %0, %1, %2, 0" : "=&v"(p0) : "v"(f0), "v"(q8[0]));
;         asm volatile("v_mfma_f32_32x32x64_f8f6f4 %0, %1, %2, 0" : "=&v"(p1) : "v"(f1), "v"(q8[0]));
;         SBAR();
;         f0 = KF8(1, 0); f1 = KF8(1, 1);
;         SBAR();
;         asm volatile("v_mfma_f32_32x32x64_f8f6f4 %0, %1, %2, %0" : "+v"(p0) : "v"(f0), "v"(q8[1]));
;         asm volatile("v_mfma_f32_32x32x64_f8f6f4 %0, %1, %2, %0" : "+v"(p1) : "v"(f1), "v"(q8[1]));
;         asm volatile("s_nop 15\n\ts_nop 15" ::: "memory");
;         SBAR();
;     ...
;         return;
.LBB0_1253:
	s_setprio 1
	s_add_i32 s76, 0, 0x10000
	v_mov_b32_e32 v2, v202
	v_mov_b32_e32 v4, v213
	s_cmp_lg_u32 s76, -1
	s_cselect_b32 s6, s76, 0
	v_lshrrev_b32_e32 v12, 1, v2
	v_lshlrev_b32_e32 v13, 1, v4
	v_bfe_u32 v5, v2, 1, 3
	v_lshl_add_u32 v2, v2, 7, s6
	v_bitop3_b32 v4, v12, v13, 7 bitop3:0x6c
	v_lshl_add_u32 v8, v4, 4, v2
	v_bitop3_b32 v4, v13, v5, 1 bitop3:0x36
	v_lshl_add_u32 v14, v4, 4, v2
	v_add_u32_e32 v4, 4, v13
	v_bitop3_b32 v4, v4, v12, 7 bitop3:0x78
	v_lshl_add_u32 v162, v4, 4, v2
	v_add_u32_e32 v4, 5, v13
	v_bitop3_b32 v4, v4, v12, 7 bitop3:0x78
	v_lshl_add_u32 v163, v4, 4, v2
	ds_read_b128 v[4:7], v8
	ds_read_b128 v[224:227], v8 offset:4096
	ds_read_b128 v[8:11], v14
	ds_read_b128 v[228:231], v14 offset:4096
	ds_read_b128 v[146:149], v162
	ds_read_b128 v[154:157], v162 offset:4096
	ds_read_b128 v[150:153], v163
	ds_read_b128 v[158:161], v163 offset:4096
	s_waitcnt lgkmcnt(4)
	v_mfma_f32_32x32x64_f8f6f4 v[162:177], v[4:11], v[178:185], 0
	s_waitcnt lgkmcnt(0)
	v_mfma_f32_32x32x64_f8f6f4 v[162:177], v[146:153], v[186:193], v[162:177]
	v_mov_b32_e32 v4, v154
	v_mov_b32_e32 v5, v155
	v_mov_b32_e32 v6, v156
	v_mov_b32_e32 v7, v157
	v_mov_b32_e32 v8, v158
	v_mov_b32_e32 v9, v159
	v_mov_b32_e32 v10, v160
	v_mov_b32_e32 v11, v161
	s_nop 0
	v_mfma_f32_32x32x64_f8f6f4 v[146:161], v[224:231], v[178:185], 0
	v_mfma_f32_32x32x64_f8f6f4 v[146:161], v[4:11], v[186:193], v[146:161]
	s_nop 15
	s_nop 5
	s_cmp_le_i32 s88, s80
	s_cbranch_scc1 .LBB0_1255
	v_cmp_gt_i32_e64 s[58:59], 50, v201
	v_cmp_gt_i32_e64 s[66:67], 51, v201
	v_cmp_gt_i32_e64 s[50:51], 49, v201
	s_and_b64 s[58:59], s[66:67], s[58:59]
	v_cmp_gt_i32_e64 s[42:43], 48, v201
	s_and_b64 s[50:51], s[58:59], s[50:51]
	v_cmp_gt_i32_e64 s[40:41], 32, v201
	s_and_b64 s[42:43], s[50:51], s[42:43]
	v_cmp_gt_i32_e64 s[38:39], 16, v201
	s_and_b64 s[40:41], s[42:43], s[40:41]
	v_cmp_gt_i32_e64 s[36:37], 0, v201
	s_and_b64 s[38:39], s[40:41], s[38:39]
	s_and_b64 s[36:37], s[38:39], s[36:37]
	v_cmp_gt_i32_e64 s[28:29], 54, v201
	v_cndmask_b32_e64 v162, v162, v210, s[36:37]
	v_cmp_gt_i32_e64 s[36:37], 55, v201
	v_cmp_gt_i32_e64 s[20:21], 53, v201
	s_and_b64 s[28:29], s[36:37], s[28:29]
	v_cmp_gt_i32_e64 s[12:13], 52, v201
	s_and_b64 s[20:21], s[28:29], s[20:21]
	v_cmp_gt_i32_e64 s[8:9], 36, v201
	v_cmp_gt_i32_e64 s[48:49], 33, v201
	v_cmp_gt_i32_e64 s[16:17], 37, v201
	v_cmp_gt_i32_e64 s[56:57], 34, v201
	v_cmp_gt_i32_e64 s[24:25], 38, v201
	v_cmp_gt_i32_e64 s[64:65], 35, v201
	v_cmp_gt_i32_e64 s[34:35], 39, v201
	s_and_b64 s[12:13], s[20:21], s[12:13]
	v_cmp_gt_i32_e64 s[6:7], 20, v201
	v_cmp_gt_i32_e64 s[46:47], 17, v201
	v_cmp_gt_i32_e64 s[14:15], 21, v201
	v_cmp_gt_i32_e64 s[54:55], 18, v201
	v_cmp_gt_i32_e64 s[22:23], 22, v201
	v_cmp_gt_i32_e64 s[62:63], 19, v201
	v_cmp_gt_i32_e64 s[30:31], 23, v201
	s_and_b64 s[64:65], s[66:67], s[64:65]
	s_and_b64 s[56:57], s[58:59], s[56:57]
	s_and_b64 s[48:49], s[50:51], s[48:49]
	s_and_b64 s[34:35], s[36:37], s[34:35]
	s_and_b64 s[24:25], s[28:29], s[24:25]
	s_and_b64 s[16:17], s[20:21], s[16:17]
	s_and_b64 s[8:9], s[12:13], s[8:9]
	v_cmp_gt_i32_e32 vcc, 4, v201
	v_cmp_gt_i32_e64 s[44:45], 1, v201
	v_cmp_gt_i32_e64 s[10:11], 5, v201
	v_cmp_gt_i32_e64 s[52:53], 2, v201
	v_cmp_gt_i32_e64 s[18:19], 6, v201
	v_cmp_gt_i32_e64 s[60:61], 3, v201
	v_cmp_gt_i32_e64 s[26:27], 7, v201
	s_and_b64 s[62:63], s[64:65], s[62:63]
	s_and_b64 s[54:55], s[56:57], s[54:55]
	s_and_b64 s[46:47], s[48:49], s[46:47]
	s_and_b64 s[30:31], s[34:35], s[30:31]
	s_and_b64 s[22:23], s[24:25], s[22:23]
	s_and_b64 s[14:15], s[16:17], s[14:15]
	s_and_b64 s[6:7], s[8:9], s[6:7]
	v_cndmask_b32_e64 v173, v173, v210, s[58:59]
	v_cndmask_b32_e64 v169, v169, v210, s[50:51]
	s_and_b64 s[58:59], s[62:63], s[60:61]
	v_cndmask_b32_e64 v165, v165, v210, s[42:43]
	s_and_b64 s[50:51], s[54:55], s[52:53]
	s_and_b64 s[42:43], s[46:47], s[44:45]
	s_and_b64 s[26:27], s[30:31], s[26:27]
	s_and_b64 s[18:19], s[22:23], s[18:19]
	s_and_b64 s[10:11], s[14:15], s[10:11]
	s_and_b64 vcc, s[6:7], vcc
	v_cndmask_b32_e64 v177, v177, v210, s[66:67]
	v_cndmask_b32_e64 v176, v176, v210, s[64:65]
	v_cndmask_b32_e64 v175, v175, v210, s[62:63]
	v_cndmask_b32_e64 v172, v172, v210, s[56:57]
	v_cndmask_b32_e64 v174, v174, v210, s[58:59]
	v_cndmask_b32_e64 v171, v171, v210, s[54:55]
	v_cndmask_b32_e64 v168, v168, v210, s[48:49]
	v_cndmask_b32_e64 v170, v170, v210, s[50:51]
	v_cndmask_b32_e64 v167, v167, v210, s[46:47]
	v_cndmask_b32_e64 v164, v164, v210, s[40:41]
	v_cndmask_b32_e64 v166, v166, v210, s[42:43]
	v_cndmask_b32_e64 v163, v163, v210, s[38:39]
	v_cndmask_b32_e64 v161, v161, v210, s[36:37]
	v_cndmask_b32_e64 v160, v160, v210, s[34:35]
	v_cndmask_b32_e64 v157, v157, v210, s[28:29]
	v_cndmask_b32_e64 v159, v159, v210, s[30:31]
	v_cndmask_b32_e64 v156, v156, v210, s[24:25]
	v_cndmask_b32_e64 v153, v153, v210, s[20:21]
	v_cndmask_b32_e64 v158, v158, v210, s[26:27]
	v_cndmask_b32_e64 v155, v155, v210, s[22:23]
	v_cndmask_b32_e64 v152, v152, v210, s[16:17]
	v_cndmask_b32_e64 v149, v149, v210, s[12:13]
	v_cndmask_b32_e64 v154, v154, v210, s[18:19]
	v_cndmask_b32_e64 v151, v151, v210, s[14:15]
	v_cndmask_b32_e64 v148, v148, v210, s[8:9]
	v_cndmask_b32_e64 v150, v150, v210, s[10:11]
	v_cndmask_b32_e64 v147, v147, v210, s[6:7]
	v_cndmask_b32_e32 v146, v146, v210, vcc

; #define SBAR() __builtin_amdgcn_sched_barrier(0)
; __device__ __forceinline__ void mask_tile_perm(f32x16& p0, f32x16& p1, int dq) {
;     const float NEG = -__builtin_inff();
; #pragma unroll
;     for (int r = 0; r < 16; ++r) { const int c = 16 * (r & 3) + (r >> 2);
;         if (dq - c < 0) p0[r] = NEG;
;         if (dq - c - 4 < 0) p1[r] = NEG; }
; }
; template <int KB, bool LOWREG = false>
; __device__ __forceinline__ void qkt_f8(f32x16& p0, f32x16& p1, const char* K_lds, int r32, int hi, const i32x8 (&q8)[2]) {
;     asm volatile("" : "+v"(r32), "+v"(hi));
;     typedef const __attribute__((address_space(3))) bf16x8* lds_f;
;     const unsigned sw = (unsigned)((r32 >> 1) & 7), base = (unsigned)(__UINTPTR_TYPE__)K_lds + (unsigned)(r32 * 128) + (unsigned)(KB * SHM_K);
;     if constexpr (LOWREG) {
;     ...
;         i32x8 f0 = KF8(0, 0), f1 = KF8(0, 1);
;         SBAR();
;         asm volatile("v_mfma_f32_32x32x64_f8f6f4 %0, %1, %2, 0" : "=&v"(p0) : "v"(f0), "v"(q8[0]));
;         asm volatile("v_mfma_f32_32x32x64_f8f6f4 %0, %1, %2, 0" : "=&v"(p1) : "v"(f1), "v"(q8[0]));
;         SBAR();
;         f0 = KF8(1, 0); f1 = KF8(1, 1);
;         SBAR();
;         asm volatile("v_mfma_f32_32x32x64_f8f6f4 %0, %1, %2, %0" : "+v"(p0) : "v"(f0), "v"(q8[1]));
;         asm volatile("v_mfma_f32_32x32x64_f8f6f4 %0, %1, %2, %0" : "+v"(p1) : "v"(f1), "v"(q8[1]));
;         asm volatile("s_nop 15\n\ts_nop 15" ::: "memory");
;         SBAR();
;     ...
;         return;
.LBB0_1271:
	s_setprio 1
	s_cmp_lg_u32 s76, -1
	v_mov_b32_e32 v4, v202
	v_mov_b32_e32 v5, v213
	s_cselect_b32 s6, s76, 0
	s_addk_i32 s6, 0x4000
	v_lshrrev_b32_e32 v12, 1, v4
	v_lshlrev_b32_e32 v14, 1, v5
	v_bfe_u32 v6, v4, 1, 3
	v_lshl_add_u32 v13, v4, 7, s6
	v_bitop3_b32 v4, v12, v14, 7 bitop3:0x6c
	v_lshl_add_u32 v8, v4, 4, v13
	v_bitop3_b32 v4, v14, v6, 1 bitop3:0x36
	v_lshl_add_u32 v15, v4, 4, v13
	v_add_u32_e32 v4, 4, v14
	v_bitop3_b32 v4, v4, v12, 7 bitop3:0x78
	v_lshl_add_u32 v162, v4, 4, v13
	v_add_u32_e32 v4, 5, v14
	v_bitop3_b32 v4, v4, v12, 7 bitop3:0x78
	v_lshl_add_u32 v163, v4, 4, v13
	ds_read_b128 v[4:7], v8
	ds_read_b128 v[224:227], v8 offset:4096
	ds_read_b128 v[8:11], v15
	ds_read_b128 v[228:231], v15 offset:4096
	ds_read_b128 v[146:149], v162
	ds_read_b128 v[154:157], v162 offset:4096
	ds_read_b128 v[150:153], v163
	ds_read_b128 v[158:161], v163 offset:4096
	s_waitcnt lgkmcnt(4)
	v_mfma_f32_32x32x64_f8f6f4 v[162:177], v[4:11], v[178:185], 0
	s_waitcnt lgkmcnt(0)
	v_mfma_f32_32x32x64_f8f6f4 v[162:177], v[146:153], v[186:193], v[162:177]
	v_mov_b32_e32 v4, v154
	v_mov_b32_e32 v5, v155
	v_mov_b32_e32 v6, v156
	v_mov_b32_e32 v7, v157
	v_mov_b32_e32 v8, v158
	v_mov_b32_e32 v9, v159
	v_mov_b32_e32 v10, v160
	v_mov_b32_e32 v11, v161
	s_nop 0
	v_mfma_f32_32x32x64_f8f6f4 v[146:161], v[224:231], v[178:185], 0
	v_mfma_f32_32x32x64_f8f6f4 v[146:161], v[4:11], v[186:193], v[146:161]
	s_nop 15
	s_nop 5
	s_add_i32 s6, s88, 64
	s_cmp_le_i32 s6, s80
	s_cbranch_scc1 .LBB0_1273
	v_subrev_u32_e32 v4, 64, v201
	v_cmp_gt_i32_e64 s[58:59], 50, v4
	v_cmp_gt_i32_e64 s[66:67], 51, v4
	v_cmp_gt_i32_e64 s[50:51], 49, v4
	s_and_b64 s[58:59], s[66:67], s[58:59]
	v_cmp_gt_i32_e64 s[42:43], 48, v4
	s_and_b64 s[50:51], s[58:59], s[50:51]
	v_cmp_gt_i32_e64 s[40:41], 32, v4
	s_and_b64 s[42:43], s[50:51], s[42:43]
	v_cmp_gt_i32_e64 s[38:39], 16, v4
	s_and_b64 s[40:41], s[42:43], s[40:41]
	v_cmp_gt_i32_e64 s[36:37], 0, v4
	s_and_b64 s[38:39], s[40:41], s[38:39]
	s_and_b64 s[36:37], s[38:39], s[36:37]
	v_cmp_gt_i32_e64 s[28:29], 54, v4
	v_cndmask_b32_e64 v162, v162, v210, s[36:37]
	v_cmp_gt_i32_e64 s[36:37], 55, v4
	v_cmp_gt_i32_e64 s[20:21], 53, v4
	s_and_b64 s[28:29], s[36:37], s[28:29]
	v_cmp_gt_i32_e64 s[12:13], 52, v4
	s_and_b64 s[20:21], s[28:29], s[20:21]
	v_cmp_gt_i32_e64 s[8:9], 36, v4
	v_cmp_gt_i32_e64 s[48:49], 33, v4
	v_cmp_gt_i32_e64 s[16:17], 37, v4
	v_cmp_gt_i32_e64 s[56:57], 34, v4
	v_cmp_gt_i32_e64 s[24:25], 38, v4
	v_cmp_gt_i32_e64 s[64:65], 35, v4
	v_cmp_gt_i32_e64 s[34:35], 39, v4
	s_and_b64 s[12:13], s[20:21], s[12:13]
	v_cmp_gt_i32_e64 s[6:7], 20, v4
	v_cmp_gt_i32_e64 s[46:47], 17, v4
	v_cmp_gt_i32_e64 s[14:15], 21, v4
	v_cmp_gt_i32_e64 s[54:55], 18, v4
	v_cmp_gt_i32_e64 s[22:23], 22, v4
	v_cmp_gt_i32_e64 s[62:63], 19, v4
	v_cmp_gt_i32_e64 s[30:31], 23, v4
	s_and_b64 s[64:65], s[66:67], s[64:65]
	s_and_b64 s[56:57], s[58:59], s[56:57]
	s_and_b64 s[48:49], s[50:51], s[48:49]
	s_and_b64 s[34:35], s[36:37], s[34:35]
	s_and_b64 s[24:25], s[28:29], s[24:25]
	s_and_b64 s[16:17], s[20:21], s[16:17]
	s_and_b64 s[8:9], s[12:13], s[8:9]
	v_cmp_gt_i32_e32 vcc, 4, v4
	v_cmp_gt_i32_e64 s[44:45], 1, v4
	v_cmp_gt_i32_e64 s[10:11], 5, v4
	v_cmp_gt_i32_e64 s[52:53], 2, v4
	v_cmp_gt_i32_e64 s[18:19], 6, v4
	v_cmp_gt_i32_e64 s[60:61], 3, v4
	v_cmp_gt_i32_e64 s[26:27], 7, v4
	s_and_b64 s[62:63], s[64:65], s[62:63]
	s_and_b64 s[54:55], s[56:57], s[54:55]
	s_and_b64 s[46:47], s[48:49], s[46:47]
	s_and_b64 s[30:31], s[34:35], s[30:31]
	s_and_b64 s[22:23], s[24:25], s[22:23]
	s_and_b64 s[14:15], s[16:17], s[14:15]
	s_and_b64 s[6:7], s[8:9], s[6:7]
	v_cndmask_b32_e64 v173, v173, v210, s[58:59]
	v_cndmask_b32_e64 v169, v169, v210, s[50:51]
	s_and_b64 s[58:59], s[62:63], s[60:61]
	v_cndmask_b32_e64 v165, v165, v210, s[42:43]
	s_and_b64 s[50:51], s[54:55], s[52:53]
	s_and_b64 s[42:43], s[46:47], s[44:45]
	s_and_b64 s[26:27], s[30:31], s[26:27]
	s_and_b64 s[18:19], s[22:23], s[18:19]
	s_and_b64 s[10:11], s[14:15], s[10:11]
	s_and_b64 vcc, s[6:7], vcc
	v_cndmask_b32_e64 v177, v177, v210, s[66:67]
	v_cndmask_b32_e64 v176, v176, v210, s[64:65]
	v_cndmask_b32_e64 v175, v175, v210, s[62:63]
	v_cndmask_b32_e64 v172, v172, v210, s[56:57]
	v_cndmask_b32_e64 v174, v174, v210, s[58:59]
	v_cndmask_b32_e64 v171, v171, v210, s[54:55]
	v_cndmask_b32_e64 v168, v168, v210, s[48:49]
	v_cndmask_b32_e64 v170, v170, v210, s[50:51]
	v_cndmask_b32_e64 v167, v167, v210, s[46:47]
	v_cndmask_b32_e64 v164, v164, v210, s[40:41]
	v_cndmask_b32_e64 v166, v166, v210, s[42:43]
	v_cndmask_b32_e64 v163, v163, v210, s[38:39]
	v_cndmask_b32_e64 v161, v161, v210, s[36:37]
	v_cndmask_b32_e64 v160, v160, v210, s[34:35]
	v_cndmask_b32_e64 v157, v157, v210, s[28:29]
	v_cndmask_b32_e64 v159, v159, v210, s[30:31]
	v_cndmask_b32_e64 v156, v156, v210, s[24:25]
	v_cndmask_b32_e64 v153, v153, v210, s[20:21]
	v_cndmask_b32_e64 v158, v158, v210, s[26:27]
	v_cndmask_b32_e64 v155, v155, v210, s[22:23]
	v_cndmask_b32_e64 v152, v152, v210, s[16:17]
	v_cndmask_b32_e64 v149, v149, v210, s[12:13]
	v_cndmask_b32_e64 v154, v154, v210, s[18:19]
	v_cndmask_b32_e64 v151, v151, v210, s[14:15]
	v_cndmask_b32_e64 v148, v148, v210, s[8:9]
	v_cndmask_b32_e64 v150, v150, v210, s[10:11]
	v_cndmask_b32_e64 v147, v147, v210, s[6:7]
	v_cndmask_b32_e32 v146, v146, v210, vcc
